# P4: diff-attention component loads moved to the row top (one round trip per row)
# baseline (speedup 1.0000x reference)
; __device__ __forceinline__ unsigned pk2(float lo, float hi) { return f2bf(lo) | (f2bf(hi) << 16); }
; __device__ __forceinline__ void p4_finalize(Frame& F, const Args& A) {
;     ...
;     for (int m = gw; m < T; m += NGW) {
;         { const int h = F.lane >> 3; const float l0 = LS[((size_t)0 * T + m) * 8 + h], l1 = LS[((size_t)1 * T + m) * 8 + h], l2 = LS[((size_t)2 * T + m) * 8 + h];
;           const float mx = fmaxf(l0, fmaxf(l1, l2)); float w0 = __expf(l0 - mx), w1 = __expf(l1 - mx), w2 = __expf(l2 - mx); const float inv = 1.0f / (w0 + w1 + w2); w0 *= inv; w1 *= inv; w2 *= inv;
;           const size_t o = (size_t)m * 1024 + 16 * F.lane; unsigned pk[8];
; #pragma unroll
;           for (int q = 0; q < 2; ++q) { const v4u a0 = *(const v4u*)(OA + o + 8 * q), a1 = *(const v4u*)(OA + (size_t)T * 1024 + o + 8 * q), a2 = *(const v4u*)(OA + (size_t)2 * T * 1024 + o + 8 * q);
; #pragma unroll
;               for (int e = 0; e < 4; ++e) { const float ylo = w0 * __uint_as_float(a0[e] << 16) + w1 * __uint_as_float(a1[e] << 16) + w2 * __uint_as_float(a2[e] << 16);
;                   const float yhi = w0 * __uint_as_float(a0[e] & 0xffff0000u) + w1 * __uint_as_float(a1[e] & 0xffff0000u) + w2 * __uint_as_float(a2[e] & 0xffff0000u); pk[4 * q + e] = pk2(ylo, yhi); } }
;           if constexpr (P5_F8) { v4u w8;
; #pragma unroll
;               for (int e = 0; e < 4; ++e) { const unsigned p0 = pk[2 * e], p1 = pk[2 * e + 1];
;                   int w = __builtin_amdgcn_cvt_pk_fp8_f32(__uint_as_float(p0 << 16) * 16.f, __uint_as_float(p0 & 0xffff0000u) * 16.f, 0, false);
;                   w = __builtin_amdgcn_cvt_pk_fp8_f32(__uint_as_float(p1 << 16) * 16.f, __uint_as_float(p1 & 0xffff0000u) * 16.f, w, true); w8[e] = (unsigned)w; }
;               *(v4u*)(WSP(unsigned char, WS_YA) + o) = w8; }
.LBB0_661:
	v_lshl_add_u64 v[22:23], s[30:31], 0, v[14:15]
	v_add_co_u32_e64 v48, s[4:5], s0, v22
	v_lshl_add_u64 v[26:27], s[30:31], 0, v[10:11]
	s_nop 0
	v_addc_co_u32_e64 v49, s[4:5], 0, v23, s[4:5]
	v_add_co_u32_e64 v42, s[4:5], s1, v22
	v_lshl_add_u64 v[28:29], s[30:31], 0, v[18:19]
	s_nop 0
	v_addc_co_u32_e64 v43, s[4:5], 0, v23, s[4:5]
	v_add_co_u32_e64 v52, s[4:5], s2, v22
	v_add_co_u32_e32 v60, vcc, 0x1a000000, v28
	s_nop 0
	v_addc_co_u32_e64 v53, s[4:5], 0, v23, s[4:5]
	v_add_co_u32_e64 v24, s[4:5], s9, v26
	v_addc_co_u32_e32 v61, vcc, 0, v29, vcc
	s_nop 0
	v_addc_co_u32_e64 v25, s[4:5], 0, v27, s[4:5]
	v_add_co_u32_e64 v26, s[4:5], s10, v26
	v_lshl_add_u64 v[40:41], s[30:31], 0, v[12:13]
	s_nop 0
	v_addc_co_u32_e64 v27, s[4:5], 0, v27, s[4:5]
	v_add_co_u32_e32 v64, vcc, 0x1a040000, v28
	v_lshl_add_u64 v[62:63], v[22:23], 0, s[38:39]
	v_lshl_add_u64 v[44:45], v[22:23], 0, s[40:41]
	v_lshl_add_u64 v[56:57], v[22:23], 0, s[42:43]
	v_add_co_u32_e64 v22, s[4:5], s15, v40
	v_addc_co_u32_e32 v65, vcc, 0, v29, vcc
	s_nop 0
	v_addc_co_u32_e64 v23, s[4:5], 0, v41, s[4:5]
	global_load_dwordx4 v[100:103], v[6:7], off
	global_load_dwordx2 v[116:117], v[24:25], off
	global_load_dwordx2 v[118:119], v[26:27], off
	global_load_dwordx2 v[104:105], v[24:25], off offset:512
	global_load_dwordx2 v[106:107], v[26:27], off offset:512
	global_load_dwordx2 v[108:109], v[24:25], off offset:1024
	global_load_dwordx2 v[110:111], v[26:27], off offset:1024
	global_load_dwordx2 v[112:113], v[24:25], off offset:1536
	global_load_dwordx2 v[114:115], v[26:27], off offset:1536
	global_load_dwordx4 v[40:43], v[42:43], off
	s_nop 0
	global_load_dwordx4 v[44:47], v[44:45], off offset:16
	s_nop 0
	global_load_dwordx4 v[48:51], v[48:49], off
	s_nop 0
	global_load_dwordx4 v[52:55], v[52:53], off
	s_nop 0
	global_load_dwordx4 v[56:59], v[56:57], off offset:16
	s_nop 0
	global_load_dword v75, v[60:61], off
	v_add_co_u32_e32 v28, vcc, 0x1a080000, v28
	v_mov_b32_e32 v2, 0
	s_nop 0
	v_addc_co_u32_e32 v29, vcc, 0, v29, vcc
	global_load_dword v76, v[64:65], off
	global_load_dword v77, v[28:29], off
	s_nop 0
	global_load_dwordx4 v[60:63], v[62:63], off offset:16
	v_mov_b32_e32 v3, 0
	v_mov_b32_e32 v4, 0
	v_mov_b32_e32 v5, 0
	v_lshl_add_u64 v[30:31], s[30:31], 0, v[16:17]
	v_mov_b32_e32 v74, 0
	s_add_i32 s8, s8, s14
	v_lshl_add_u64 v[10:11], v[10:11], 0, s[18:19]
	v_lshl_add_u64 v[12:13], v[12:13], 0, s[22:23]
	v_lshl_add_u64 v[14:15], v[14:15], 0, s[18:19]
	v_lshl_add_u64 v[16:17], v[16:17], 0, s[22:23]
	v_lshl_add_u64 v[18:19], v[18:19], 0, s[36:37]
	s_cmpk_lt_i32 s8, 0x2000
	s_waitcnt vmcnt(8)
	v_lshlrev_b32_e32 v78, 16, v40
	v_and_b32_e32 v79, 0xffff0000, v40
	v_lshlrev_b32_e32 v80, 16, v41
	v_and_b32_e32 v81, 0xffff0000, v41
	v_lshlrev_b32_e32 v82, 16, v42
	v_and_b32_e32 v83, 0xffff0000, v42
	v_lshlrev_b32_e32 v84, 16, v43
	v_and_b32_e32 v85, 0xffff0000, v43
	s_waitcnt vmcnt(7)
	v_lshlrev_b32_e32 v86, 16, v44
	s_waitcnt vmcnt(1)
	v_max3_f32 v94, v75, v76, v77
	v_and_b32_e32 v87, 0xffff0000, v44
	v_lshlrev_b32_e32 v88, 16, v45
	v_and_b32_e32 v89, 0xffff0000, v45
	v_lshlrev_b32_e32 v90, 16, v46
	v_and_b32_e32 v91, 0xffff0000, v46
	v_lshlrev_b32_e32 v92, 16, v47
	v_lshlrev_b32_e32 v29, 16, v48
	v_lshlrev_b32_e32 v28, 16, v52
	v_and_b32_e32 v41, 0xffff0000, v48
	v_and_b32_e32 v40, 0xffff0000, v52
	v_lshlrev_b32_e32 v43, 16, v49
	v_lshlrev_b32_e32 v42, 16, v53
	v_and_b32_e32 v45, 0xffff0000, v49
	v_and_b32_e32 v44, 0xffff0000, v53
	v_lshlrev_b32_e32 v49, 16, v50
	v_lshlrev_b32_e32 v48, 16, v54
	v_and_b32_e32 v53, 0xffff0000, v50
	v_and_b32_e32 v52, 0xffff0000, v54
	v_lshlrev_b32_e32 v64, 16, v55
	v_and_b32_e32 v50, 0xffff0000, v55
	v_lshlrev_b32_e32 v46, 16, v56
	v_and_b32_e32 v54, 0xffff0000, v56
	v_lshlrev_b32_e32 v56, 16, v57
	v_and_b32_e32 v66, 0xffff0000, v57
	v_and_b32_e32 v93, 0xffff0000, v47
	s_waitcnt vmcnt(0)
	v_lshlrev_b32_e32 v47, 16, v60
	v_and_b32_e32 v55, 0xffff0000, v60
	v_lshlrev_b32_e32 v57, 16, v61
	v_and_b32_e32 v67, 0xffff0000, v61
	v_sub_f32_e32 v60, v75, v94
	v_sub_f32_e32 v61, v76, v94
	v_lshlrev_b32_e32 v70, 16, v59
	v_and_b32_e32 v72, 0xffff0000, v59
	v_lshlrev_b32_e32 v69, 16, v62
	v_and_b32_e32 v59, 0xffff0000, v62
	v_lshlrev_b32_e32 v71, 16, v63
	v_and_b32_e32 v73, 0xffff0000, v63
	v_sub_f32_e32 v62, v77, v94
	v_mul_f32_e32 v60, 0x3fb8aa3b, v60
	v_mul_f32_e32 v63, 0x3fb8aa3b, v61
	v_mul_f32_e32 v62, 0x3fb8aa3b, v62
	v_exp_f32_e32 v61, v60
	v_exp_f32_e32 v63, v63
	v_exp_f32_e32 v60, v62
	v_lshlrev_b32_e32 v65, 16, v51
	v_and_b32_e32 v51, 0xffff0000, v51
	v_add_f32_e32 v62, v61, v63
	v_add_f32_e32 v62, v60, v62
	v_div_scale_f32 v75, s[4:5], v62, v62, 1.0
	v_rcp_f32_e32 v77, v75
	v_div_scale_f32 v76, vcc, 1.0, v62, 1.0
	v_lshlrev_b32_e32 v68, 16, v58
	v_fma_f32 v94, -v75, v77, 1.0
	v_fmac_f32_e32 v77, v94, v77
	v_mul_f32_e32 v94, v76, v77
	v_fma_f32 v95, -v75, v94, v76
	v_fmac_f32_e32 v94, v95, v77
	v_fma_f32 v75, -v75, v94, v76
	v_div_fmas_f32 v75, v75, v77, v94
	v_div_fixup_f32 v62, v75, v62, 1.0
	v_and_b32_e32 v58, 0xffff0000, v58
	v_pk_mul_f32 v[60:61], v[60:61], v[62:63] op_sel_hi:[1,0]
	v_mul_f32_e32 v75, v63, v62
	v_pk_mul_f32 v[28:29], v[60:61], v[28:29]
	v_pk_mul_f32 v[40:41], v[60:61], v[40:41]
	v_pk_mul_f32 v[42:43], v[60:61], v[42:43]
	v_pk_mul_f32 v[44:45], v[60:61], v[44:45]
	v_pk_mul_f32 v[48:49], v[60:61], v[48:49]
	v_pk_mul_f32 v[52:53], v[60:61], v[52:53]
	v_pk_mul_f32 v[62:63], v[60:61], v[64:65]
	v_pk_mul_f32 v[50:51], v[60:61], v[50:51]
	v_pk_mul_f32 v[46:47], v[60:61], v[46:47]
	v_pk_mul_f32 v[54:55], v[60:61], v[54:55]
	v_pk_mul_f32 v[64:65], v[60:61], v[66:67]
	v_pk_mul_f32 v[66:67], v[60:61], v[68:69]
; __device__ __forceinline__ unsigned pk2(float lo, float hi) { return f2bf(lo) | (f2bf(hi) << 16); }
; __device__ __forceinline__ void p4_finalize(Frame& F, const Args& A) {
;     ...
;               for (int e = 0; e < 4; ++e) { const float ylo = w0 * __uint_as_float(a0[e] << 16) + w1 * __uint_as_float(a1[e] << 16) + w2 * __uint_as_float(a2[e] << 16);
;                   const float yhi = w0 * __uint_as_float(a0[e] & 0xffff0000u) + w1 * __uint_as_float(a1[e] & 0xffff0000u) + w2 * __uint_as_float(a2[e] & 0xffff0000u); pk[4 * q + e] = pk2(ylo, yhi); } }
;           if constexpr (P5_F8) { v4u w8;
; #pragma unroll
;               for (int e = 0; e < 4; ++e) { const unsigned p0 = pk[2 * e], p1 = pk[2 * e + 1];
;                   int w = __builtin_amdgcn_cvt_pk_fp8_f32(__uint_as_float(p0 << 16) * 16.f, __uint_as_float(p0 & 0xffff0000u) * 16.f, 0, false);
;                   w = __builtin_amdgcn_cvt_pk_fp8_f32(__uint_as_float(p1 << 16) * 16.f, __uint_as_float(p1 & 0xffff0000u) * 16.f, w, true); w8[e] = (unsigned)w; }
;               *(v4u*)(WSP(unsigned char, WS_YA) + o) = w8; }
;           else { bf16* ya = WSP(bf16, WS_YA) + o; *(v4u*)ya = (v4u){pk[0], pk[1], pk[2], pk[3]}; *(v4u*)(ya + 8) = (v4u){pk[4], pk[5], pk[6], pk[7]}; } }
; #pragma unroll
;         for (int h = 0; h < 4; ++h) { const size_t o = (size_t)m * 1024 + h * 256 + 4 * F.lane;
;             const v2u b0 = *(const v2u*)(OB + o), b1 = *(const v2u*)(OB + (size_t)T * 1024 + o);
;             const f32x4 v = (f32x4){__uint_as_float(b0.x << 16), __uint_as_float(b0.x & 0xffff0000u), __uint_as_float(b0.y << 16), __uint_as_float(b0.y & 0xffff0000u)}
;                           - (f32x4){__uint_as_float(b1.x << 16), __uint_as_float(b1.x & 0xffff0000u), __uint_as_float(b1.y << 16), __uint_as_float(b1.y & 0xffff0000u)} * lam;
;             const float ss = wave_sum((v.x * v.x + v.y * v.y) + (v.z * v.z + v.w * v.w)); const float rstd = 1.0f / sqrtf(ss * (1.0f / 256.0f) + EPS);
	v_pk_mul_f32 v[58:59], v[60:61], v[58:59]
	v_fma_f32 v29, v75, v78, v29
	v_fma_f32 v41, v75, v79, v41
	v_fma_f32 v43, v75, v80, v43
	v_fma_f32 v45, v75, v81, v45
	v_fma_f32 v49, v75, v82, v49
	v_fma_f32 v53, v75, v83, v53
	v_fma_f32 v51, v75, v85, v51
	v_fma_f32 v47, v75, v86, v47
	v_fma_f32 v55, v75, v87, v55
	v_fma_f32 v67, v75, v90, v67
	v_fma_f32 v59, v75, v91, v59
	v_fma_f32 v63, v75, v84, v63
	v_add_f32_e32 v28, v28, v29
	v_add_f32_e32 v29, v40, v41
	v_add_f32_e32 v40, v42, v43
	v_add_f32_e32 v41, v44, v45
	v_add_f32_e32 v42, v48, v49
	v_add_f32_e32 v43, v52, v53
	v_add_f32_e32 v45, v50, v51
	v_add_f32_e32 v46, v46, v47
	v_add_f32_e32 v47, v54, v55
	v_add_f32_e32 v50, v66, v67
	v_add_f32_e32 v51, v58, v59
	v_add_f32_e32 v44, v62, v63
	v_bfe_u32 v54, v28, 16, 1
	v_bfe_u32 v55, v29, 16, 1
	v_bfe_u32 v58, v42, 16, 1
	v_bfe_u32 v59, v43, 16, 1
	v_bfe_u32 v62, v46, 16, 1
	v_bfe_u32 v63, v47, 16, 1
	v_bfe_u32 v66, v50, 16, 1
	v_bfe_u32 v67, v51, 16, 1
	v_pk_mul_f32 v[56:57], v[60:61], v[56:57]
	v_pk_mul_f32 v[68:69], v[60:61], v[70:71]
	v_pk_mul_f32 v[60:61], v[60:61], v[72:73]
	v_add3_u32 v28, v28, v54, s3
	v_add3_u32 v29, v29, v55, s3
	v_add3_u32 v42, v42, v58, s3
	v_add3_u32 v43, v43, v59, s3
	v_add3_u32 v46, v46, v62, s3
	v_add3_u32 v47, v47, v63, s3
	v_add3_u32 v50, v50, v66, s3
	v_add3_u32 v51, v51, v67, s3
	v_fma_f32 v57, v75, v88, v57
	v_fma_f32 v65, v75, v89, v65
	v_fma_f32 v69, v75, v92, v69
	v_fma_f32 v61, v75, v93, v61
	v_and_b32_e32 v29, 0xffff0000, v29
	v_and_b32_e32 v43, 0xffff0000, v43
	v_and_b32_e32 v47, 0xffff0000, v47
	v_and_b32_e32 v51, 0xffff0000, v51
	v_and_b32_e32 v28, 0xffff0000, v28
	v_and_b32_e32 v42, 0xffff0000, v42
	v_and_b32_e32 v46, 0xffff0000, v46
	v_and_b32_e32 v50, 0xffff0000, v50
	v_add_f32_e32 v48, v56, v57
	v_add_f32_e32 v49, v64, v65
	v_add_f32_e32 v52, v68, v69
	v_add_f32_e32 v53, v60, v61
	v_mul_f32_e32 v28, 0x41800000, v28
	v_mul_f32_e32 v29, 0x41800000, v29
	v_mul_f32_e32 v42, 0x41800000, v42
	v_mul_f32_e32 v43, 0x41800000, v43
	v_mul_f32_e32 v46, 0x41800000, v46
	v_mul_f32_e32 v47, 0x41800000, v47
	v_mul_f32_e32 v50, 0x41800000, v50
	v_mul_f32_e32 v51, 0x41800000, v51
	v_bfe_u32 v56, v40, 16, 1
	v_bfe_u32 v57, v41, 16, 1
	v_bfe_u32 v60, v44, 16, 1
	v_bfe_u32 v61, v45, 16, 1
	v_bfe_u32 v64, v48, 16, 1
	v_bfe_u32 v65, v49, 16, 1
	v_bfe_u32 v68, v52, 16, 1
	v_bfe_u32 v69, v53, 16, 1
	v_cvt_pk_fp8_f32 v2, v28, v29
	v_cvt_pk_fp8_f32 v3, v42, v43
	v_cvt_pk_fp8_f32 v4, v46, v47
	v_cvt_pk_fp8_f32 v5, v50, v51
	v_add3_u32 v40, v40, v56, s3
	v_add3_u32 v41, v41, v57, s3
	v_add3_u32 v44, v44, v60, s3
	v_add3_u32 v45, v45, v61, s3
	v_add3_u32 v48, v48, v64, s3
	v_add3_u32 v49, v49, v65, s3
	v_add3_u32 v52, v52, v68, s3
	v_add3_u32 v53, v53, v69, s3
	v_and_b32_e32 v41, 0xffff0000, v41
	v_and_b32_e32 v45, 0xffff0000, v45
	v_and_b32_e32 v49, 0xffff0000, v49
	v_and_b32_e32 v53, 0xffff0000, v53
	v_and_b32_e32 v40, 0xffff0000, v40
	v_and_b32_e32 v44, 0xffff0000, v44
	v_and_b32_e32 v48, 0xffff0000, v48
	v_and_b32_e32 v52, 0xffff0000, v52
	v_mul_f32_e32 v40, 0x41800000, v40
	v_mul_f32_e32 v41, 0x41800000, v41
	v_mul_f32_e32 v44, 0x41800000, v44
	v_mul_f32_e32 v45, 0x41800000, v45
	v_mul_f32_e32 v48, 0x41800000, v48
	v_mul_f32_e32 v49, 0x41800000, v49
	v_mul_f32_e32 v52, 0x41800000, v52
	v_mul_f32_e32 v53, 0x41800000, v53
	v_cvt_pk_fp8_f32 v2, v40, v41 op_sel:[0,0,1]
	v_cvt_pk_fp8_f32 v3, v44, v45 op_sel:[0,0,1]
	v_cvt_pk_fp8_f32 v4, v48, v49 op_sel:[0,0,1]
	v_cvt_pk_fp8_f32 v5, v52, v53 op_sel:[0,0,1]
	v_mov_b32_e32 v46, 0
	global_store_dwordx4 v[30:31], v[2:5], off
	s_nop 1
	v_mov_b64_e32 v[28:29], v[116:117]
	v_lshlrev_b32_e32 v40, 16, v28
	v_and_b32_e32 v41, 0xffff0000, v28
	v_lshlrev_b32_e32 v28, 16, v29
	v_and_b32_e32 v29, 0xffff0000, v29
	v_mov_b64_e32 v[30:31], v[118:119]
	v_lshlrev_b32_e32 v42, 16, v30
	v_and_b32_e32 v43, 0xffff0000, v30
	v_lshlrev_b32_e32 v30, 16, v31
	v_and_b32_e32 v31, 0xffff0000, v31
	v_pk_fma_f32 v[40:41], v[8:9], v[42:43], v[40:41] neg_lo:[1,0,0] neg_hi:[1,0,0]
	v_pk_fma_f32 v[28:29], v[20:21], v[30:31], v[28:29]
	v_pk_mul_f32 v[42:43], v[40:41], v[40:41]
	v_pk_mul_f32 v[30:31], v[28:29], v[28:29]
	s_nop 0
	v_pk_mov_b32 v[44:45], v[42:43], v[30:31] op_sel:[1,0]
	v_mov_b32_e32 v43, v31
	v_pk_add_f32 v[30:31], v[44:45], v[42:43]
	s_nop 0
	v_add_f32_e32 v30, v30, v31
	ds_bpermute_b32 v31, v32, v30
	s_waitcnt lgkmcnt(0)
	v_add_f32_e32 v30, v30, v31
	ds_bpermute_b32 v31, v33, v30
	s_waitcnt lgkmcnt(0)
	v_add_f32_e32 v30, v30, v31
	ds_bpermute_b32 v31, v34, v30
	s_waitcnt lgkmcnt(0)
	v_add_f32_e32 v30, v30, v31
	ds_bpermute_b32 v31, v35, v30
	s_waitcnt lgkmcnt(0)
	v_add_f32_e32 v30, v30, v31
	ds_bpermute_b32 v31, v36, v30
	s_waitcnt lgkmcnt(0)
	v_add_f32_e32 v30, v30, v31
	ds_bpermute_b32 v31, v37, v30
	s_waitcnt lgkmcnt(0)
; __device__ __forceinline__ void p4_finalize(Frame& F, const Args& A) {
;     ...
;         for (int h = 0; h < 4; ++h) { const size_t o = (size_t)m * 1024 + h * 256 + 4 * F.lane;
;             const v2u b0 = *(const v2u*)(OB + o), b1 = *(const v2u*)(OB + (size_t)T * 1024 + o);
;             const f32x4 v = (f32x4){__uint_as_float(b0.x << 16), __uint_as_float(b0.x & 0xffff0000u), __uint_as_float(b0.y << 16), __uint_as_float(b0.y & 0xffff0000u)}
;                           - (f32x4){__uint_as_float(b1.x << 16), __uint_as_float(b1.x & 0xffff0000u), __uint_as_float(b1.y << 16), __uint_as_float(b1.y & 0xffff0000u)} * lam;
;             const float ss = wave_sum((v.x * v.x + v.y * v.y) + (v.z * v.z + v.w * v.w)); const float rstd = 1.0f / sqrtf(ss * (1.0f / 256.0f) + EPS);
;             const f32x4 g = *(const f32x4*)(A.in[I_SUBG] + 4 * F.lane); const f32x4 y = v * rstd * g * (1.0f - LAMBDA_INIT);
;             if constexpr (P5_F8) { int w = __builtin_amdgcn_cvt_pk_fp8_f32(y.x * 16.f, y.y * 16.f, 0, false); w = __builtin_amdgcn_cvt_pk_fp8_f32(y.z * 16.f, y.w * 16.f, w, true); *(int*)(WSP(unsigned char, WS_YB) + o) = w; }
	v_add_f32_e32 v30, v30, v31
	v_fmamk_f32 v30, v30, 0x3b800000, v38
	v_mul_f32_e32 v31, 0x4f800000, v30
	v_cmp_gt_f32_e32 vcc, s11, v30
	s_nop 1
	v_cndmask_b32_e32 v30, v30, v31, vcc
	v_sqrt_f32_e32 v31, v30
	s_nop 0
	v_add_u32_e32 v42, -1, v31
	v_add_u32_e32 v43, 1, v31
	v_fma_f32 v44, -v42, v31, v30
	v_fma_f32 v45, -v43, v31, v30
	v_cmp_ge_f32_e64 s[4:5], 0, v44
	s_nop 1
	v_cndmask_b32_e64 v31, v31, v42, s[4:5]
	v_cmp_lt_f32_e64 s[4:5], 0, v45
	s_nop 1
	v_cndmask_b32_e64 v31, v31, v43, s[4:5]
	v_mul_f32_e32 v42, 0x37800000, v31
	v_cndmask_b32_e32 v31, v31, v42, vcc
	v_cmp_class_f32_e32 vcc, v30, v39
	s_nop 1
	v_cndmask_b32_e32 v30, v31, v30, vcc
	v_div_scale_f32 v31, s[4:5], v30, v30, 1.0
	v_rcp_f32_e32 v43, v31
	v_div_scale_f32 v42, vcc, 1.0, v30, 1.0
	v_fma_f32 v44, -v31, v43, 1.0
	v_fmac_f32_e32 v43, v44, v43
	v_mul_f32_e32 v44, v42, v43
	v_fma_f32 v45, -v31, v44, v42
	v_fmac_f32_e32 v44, v45, v43
	v_fma_f32 v31, -v31, v44, v42
	v_div_fmas_f32 v31, v31, v43, v44
	v_div_fixup_f32 v30, v31, v30, 1.0
	v_pk_mul_f32 v[28:29], v[28:29], v[30:31] op_sel_hi:[1,0]
	v_pk_mul_f32 v[30:31], v[40:41], v[30:31] op_sel_hi:[1,0]
	v_mov_b64_e32 v[2:3], v[100:101]
	v_mov_b64_e32 v[4:5], v[102:103]
	v_pk_mul_f32 v[4:5], v[4:5], v[28:29]
	v_pk_mul_f32 v[2:3], v[2:3], v[30:31]
	v_pk_mul_f32 v[4:5], v[4:5], s[44:45] op_sel_hi:[1,0]
	v_pk_mul_f32 v[2:3], v[2:3], s[44:45] op_sel_hi:[1,0]
	v_mul_f32_e32 v4, 0x41800000, v4
	v_mul_f32_e32 v2, 0x41800000, v2
	v_mul_f32_e32 v3, 0x41800000, v3
	v_cvt_pk_fp8_f32 v74, v2, v3
	v_mul_f32_e32 v5, 0x41800000, v5
	v_cvt_pk_fp8_f32 v74, v4, v5 op_sel:[0,0,1]
	global_store_dword v[22:23], v74, off
	s_nop 1
	v_mov_b64_e32 v[28:29], v[104:105]
	v_lshlrev_b32_e32 v40, 16, v28
	v_and_b32_e32 v41, 0xffff0000, v28
	v_lshlrev_b32_e32 v28, 16, v29
	v_and_b32_e32 v29, 0xffff0000, v29
	v_mov_b64_e32 v[30:31], v[106:107]
	v_lshlrev_b32_e32 v42, 16, v30
	v_and_b32_e32 v43, 0xffff0000, v30
	v_lshlrev_b32_e32 v30, 16, v31
	v_and_b32_e32 v31, 0xffff0000, v31
	v_pk_fma_f32 v[40:41], v[8:9], v[42:43], v[40:41] neg_lo:[1,0,0] neg_hi:[1,0,0]
	v_pk_fma_f32 v[28:29], v[20:21], v[30:31], v[28:29]
	v_pk_mul_f32 v[42:43], v[40:41], v[40:41]
	v_pk_mul_f32 v[30:31], v[28:29], v[28:29]
	s_nop 0
	v_pk_mov_b32 v[44:45], v[42:43], v[30:31] op_sel:[1,0]
	v_mov_b32_e32 v43, v31
	v_pk_add_f32 v[30:31], v[44:45], v[42:43]
	s_nop 0
	v_add_f32_e32 v30, v30, v31
	ds_bpermute_b32 v31, v32, v30
	s_waitcnt lgkmcnt(0)
	v_add_f32_e32 v30, v30, v31
	ds_bpermute_b32 v31, v33, v30
	s_waitcnt lgkmcnt(0)
	v_add_f32_e32 v30, v30, v31
	ds_bpermute_b32 v31, v34, v30
	s_waitcnt lgkmcnt(0)
	v_add_f32_e32 v30, v30, v31
	ds_bpermute_b32 v31, v35, v30
	s_waitcnt lgkmcnt(0)
	v_add_f32_e32 v30, v30, v31
	ds_bpermute_b32 v31, v36, v30
	s_waitcnt lgkmcnt(0)
	v_add_f32_e32 v30, v30, v31
	ds_bpermute_b32 v31, v37, v30
	s_waitcnt lgkmcnt(0)
	v_add_f32_e32 v30, v30, v31
	v_fmamk_f32 v30, v30, 0x3b800000, v38
	v_mul_f32_e32 v31, 0x4f800000, v30
	v_cmp_gt_f32_e32 vcc, s11, v30
	s_nop 1
	v_cndmask_b32_e32 v30, v30, v31, vcc
	v_sqrt_f32_e32 v31, v30
	s_nop 0
	v_add_u32_e32 v42, -1, v31
	v_add_u32_e32 v43, 1, v31
	v_fma_f32 v44, -v42, v31, v30
	v_fma_f32 v45, -v43, v31, v30
	v_cmp_ge_f32_e64 s[4:5], 0, v44
	s_nop 1
	v_cndmask_b32_e64 v31, v31, v42, s[4:5]
	v_cmp_lt_f32_e64 s[4:5], 0, v45
	s_nop 1
	v_cndmask_b32_e64 v31, v31, v43, s[4:5]
	v_mul_f32_e32 v42, 0x37800000, v31
	v_cndmask_b32_e32 v31, v31, v42, vcc
	v_cmp_class_f32_e32 vcc, v30, v39
	s_nop 1
	v_cndmask_b32_e32 v30, v31, v30, vcc
	v_div_scale_f32 v31, s[4:5], v30, v30, 1.0
	v_rcp_f32_e32 v43, v31
	v_div_scale_f32 v42, vcc, 1.0, v30, 1.0
	v_fma_f32 v44, -v31, v43, 1.0
	v_fmac_f32_e32 v43, v44, v43
	v_mul_f32_e32 v44, v42, v43
	v_fma_f32 v45, -v31, v44, v42
	v_fmac_f32_e32 v44, v45, v43
	v_fma_f32 v31, -v31, v44, v42
	v_div_fmas_f32 v31, v31, v43, v44
	v_div_fixup_f32 v30, v31, v30, 1.0
	v_pk_mul_f32 v[28:29], v[28:29], v[30:31] op_sel_hi:[1,0]
	v_pk_mul_f32 v[30:31], v[40:41], v[30:31] op_sel_hi:[1,0]
	v_mov_b64_e32 v[2:3], v[100:101]
	v_mov_b64_e32 v[4:5], v[102:103]
	v_pk_mul_f32 v[4:5], v[4:5], v[28:29]
	v_pk_mul_f32 v[2:3], v[2:3], v[30:31]
	v_pk_mul_f32 v[4:5], v[4:5], s[44:45] op_sel_hi:[1,0]
	v_pk_mul_f32 v[2:3], v[2:3], s[44:45] op_sel_hi:[1,0]
	v_mul_f32_e32 v4, 0x41800000, v4
	v_mul_f32_e32 v2, 0x41800000, v2
	v_mul_f32_e32 v3, 0x41800000, v3
	v_cvt_pk_fp8_f32 v46, v2, v3
	v_mul_f32_e32 v5, 0x41800000, v5
	v_cvt_pk_fp8_f32 v46, v4, v5 op_sel:[0,0,1]
	global_store_dword v[22:23], v46, off offset:256
	s_nop 1
	v_mov_b32_e32 v46, 0
	v_mov_b64_e32 v[28:29], v[108:109]
	v_lshlrev_b32_e32 v40, 16, v28
	v_and_b32_e32 v41, 0xffff0000, v28
	v_lshlrev_b32_e32 v28, 16, v29
	v_and_b32_e32 v29, 0xffff0000, v29
	v_mov_b64_e32 v[30:31], v[110:111]
	v_lshlrev_b32_e32 v42, 16, v30
	v_and_b32_e32 v43, 0xffff0000, v30
	v_lshlrev_b32_e32 v30, 16, v31
	v_and_b32_e32 v31, 0xffff0000, v31
	v_pk_fma_f32 v[40:41], v[8:9], v[42:43], v[40:41] neg_lo:[1,0,0] neg_hi:[1,0,0]
	v_pk_fma_f32 v[28:29], v[20:21], v[30:31], v[28:29]
	v_pk_mul_f32 v[42:43], v[40:41], v[40:41]
	v_pk_mul_f32 v[30:31], v[28:29], v[28:29]
	s_nop 0
	v_pk_mov_b32 v[44:45], v[42:43], v[30:31] op_sel:[1,0]
	v_mov_b32_e32 v43, v31
	v_pk_add_f32 v[30:31], v[44:45], v[42:43]
	s_nop 0
	v_add_f32_e32 v30, v30, v31
	ds_bpermute_b32 v31, v32, v30
	s_waitcnt lgkmcnt(0)
; __device__ __forceinline__ void p4_finalize(Frame& F, const Args& A) {
;     ...
;         for (int h = 0; h < 4; ++h) { const size_t o = (size_t)m * 1024 + h * 256 + 4 * F.lane;
;             const v2u b0 = *(const v2u*)(OB + o), b1 = *(const v2u*)(OB + (size_t)T * 1024 + o);
;             const f32x4 v = (f32x4){__uint_as_float(b0.x << 16), __uint_as_float(b0.x & 0xffff0000u), __uint_as_float(b0.y << 16), __uint_as_float(b0.y & 0xffff0000u)}
;                           - (f32x4){__uint_as_float(b1.x << 16), __uint_as_float(b1.x & 0xffff0000u), __uint_as_float(b1.y << 16), __uint_as_float(b1.y & 0xffff0000u)} * lam;
;             const float ss = wave_sum((v.x * v.x + v.y * v.y) + (v.z * v.z + v.w * v.w)); const float rstd = 1.0f / sqrtf(ss * (1.0f / 256.0f) + EPS);
;             const f32x4 g = *(const f32x4*)(A.in[I_SUBG] + 4 * F.lane); const f32x4 y = v * rstd * g * (1.0f - LAMBDA_INIT);
;             if constexpr (P5_F8) { int w = __builtin_amdgcn_cvt_pk_fp8_f32(y.x * 16.f, y.y * 16.f, 0, false); w = __builtin_amdgcn_cvt_pk_fp8_f32(y.z * 16.f, y.w * 16.f, w, true); *(int*)(WSP(unsigned char, WS_YB) + o) = w; }
	v_add_f32_e32 v30, v30, v31
	ds_bpermute_b32 v31, v33, v30
	s_waitcnt lgkmcnt(0)
	v_add_f32_e32 v30, v30, v31
	ds_bpermute_b32 v31, v34, v30
	s_waitcnt lgkmcnt(0)
	v_add_f32_e32 v30, v30, v31
	ds_bpermute_b32 v31, v35, v30
	s_waitcnt lgkmcnt(0)
	v_add_f32_e32 v30, v30, v31
	ds_bpermute_b32 v31, v36, v30
	s_waitcnt lgkmcnt(0)
	v_add_f32_e32 v30, v30, v31
	ds_bpermute_b32 v31, v37, v30
	s_waitcnt lgkmcnt(0)
	v_add_f32_e32 v30, v30, v31
	v_fmamk_f32 v30, v30, 0x3b800000, v38
	v_mul_f32_e32 v31, 0x4f800000, v30
	v_cmp_gt_f32_e32 vcc, s11, v30
	s_nop 1
	v_cndmask_b32_e32 v30, v30, v31, vcc
	v_sqrt_f32_e32 v31, v30
	s_nop 0
	v_add_u32_e32 v42, -1, v31
	v_add_u32_e32 v43, 1, v31
	v_fma_f32 v44, -v42, v31, v30
	v_fma_f32 v45, -v43, v31, v30
	v_cmp_ge_f32_e64 s[4:5], 0, v44
	s_nop 1
	v_cndmask_b32_e64 v31, v31, v42, s[4:5]
	v_cmp_lt_f32_e64 s[4:5], 0, v45
	s_nop 1
	v_cndmask_b32_e64 v31, v31, v43, s[4:5]
	v_mul_f32_e32 v42, 0x37800000, v31
	v_cndmask_b32_e32 v31, v31, v42, vcc
	v_cmp_class_f32_e32 vcc, v30, v39
	s_nop 1
	v_cndmask_b32_e32 v30, v31, v30, vcc
	v_div_scale_f32 v31, s[4:5], v30, v30, 1.0
	v_rcp_f32_e32 v43, v31
	v_div_scale_f32 v42, vcc, 1.0, v30, 1.0
	v_fma_f32 v44, -v31, v43, 1.0
	v_fmac_f32_e32 v43, v44, v43
	v_mul_f32_e32 v44, v42, v43
	v_fma_f32 v45, -v31, v44, v42
	v_fmac_f32_e32 v44, v45, v43
	v_fma_f32 v31, -v31, v44, v42
	v_div_fmas_f32 v31, v31, v43, v44
	v_div_fixup_f32 v30, v31, v30, 1.0
	v_pk_mul_f32 v[28:29], v[28:29], v[30:31] op_sel_hi:[1,0]
	v_pk_mul_f32 v[30:31], v[40:41], v[30:31] op_sel_hi:[1,0]
	v_mov_b64_e32 v[2:3], v[100:101]
	v_mov_b64_e32 v[4:5], v[102:103]
	v_pk_mul_f32 v[4:5], v[4:5], v[28:29]
	v_pk_mul_f32 v[2:3], v[2:3], v[30:31]
	v_pk_mul_f32 v[4:5], v[4:5], s[44:45] op_sel_hi:[1,0]
	v_pk_mul_f32 v[2:3], v[2:3], s[44:45] op_sel_hi:[1,0]
	v_mul_f32_e32 v4, 0x41800000, v4
	v_mul_f32_e32 v2, 0x41800000, v2
	v_mul_f32_e32 v3, 0x41800000, v3
	v_cvt_pk_fp8_f32 v46, v2, v3
	v_mul_f32_e32 v5, 0x41800000, v5
	v_mov_b32_e32 v42, 0
	v_cvt_pk_fp8_f32 v46, v4, v5 op_sel:[0,0,1]
	global_store_dword v[22:23], v46, off offset:512
	s_nop 1
	v_mov_b64_e32 v[24:25], v[112:113]
	v_lshlrev_b32_e32 v28, 16, v24
	v_and_b32_e32 v29, 0xffff0000, v24
	v_lshlrev_b32_e32 v24, 16, v25
	v_and_b32_e32 v25, 0xffff0000, v25
	v_mov_b64_e32 v[26:27], v[114:115]
	v_lshlrev_b32_e32 v30, 16, v26
	v_and_b32_e32 v31, 0xffff0000, v26
	v_lshlrev_b32_e32 v26, 16, v27
	v_and_b32_e32 v27, 0xffff0000, v27
	v_pk_fma_f32 v[28:29], v[8:9], v[30:31], v[28:29] neg_lo:[1,0,0] neg_hi:[1,0,0]
	v_pk_fma_f32 v[24:25], v[20:21], v[26:27], v[24:25]
	v_pk_mul_f32 v[30:31], v[28:29], v[28:29]
	v_pk_mul_f32 v[26:27], v[24:25], v[24:25]
	s_nop 0
	v_pk_mov_b32 v[40:41], v[30:31], v[26:27] op_sel:[1,0]
	v_mov_b32_e32 v31, v27
	v_pk_add_f32 v[26:27], v[40:41], v[30:31]
	s_nop 0
	v_add_f32_e32 v26, v26, v27
	ds_bpermute_b32 v27, v32, v26
	s_waitcnt lgkmcnt(0)
	v_add_f32_e32 v26, v26, v27
	ds_bpermute_b32 v27, v33, v26
	s_waitcnt lgkmcnt(0)
	v_add_f32_e32 v26, v26, v27
	ds_bpermute_b32 v27, v34, v26
	s_waitcnt lgkmcnt(0)
	v_add_f32_e32 v26, v26, v27
	ds_bpermute_b32 v27, v35, v26
	s_waitcnt lgkmcnt(0)
	v_add_f32_e32 v26, v26, v27
	ds_bpermute_b32 v27, v36, v26
	s_waitcnt lgkmcnt(0)
	v_add_f32_e32 v26, v26, v27
	ds_bpermute_b32 v27, v37, v26
	s_waitcnt lgkmcnt(0)
	v_add_f32_e32 v26, v26, v27
	v_fmamk_f32 v26, v26, 0x3b800000, v38
	v_mul_f32_e32 v27, 0x4f800000, v26
	v_cmp_gt_f32_e32 vcc, s11, v26
	s_nop 1
	v_cndmask_b32_e32 v26, v26, v27, vcc
	v_sqrt_f32_e32 v27, v26
	s_nop 0
	v_add_u32_e32 v30, -1, v27
	v_add_u32_e32 v31, 1, v27
	v_fma_f32 v40, -v30, v27, v26
	v_fma_f32 v41, -v31, v27, v26
	v_cmp_ge_f32_e64 s[4:5], 0, v40
	s_nop 1
	v_cndmask_b32_e64 v27, v27, v30, s[4:5]
	v_cmp_lt_f32_e64 s[4:5], 0, v41
	s_nop 1
	v_cndmask_b32_e64 v27, v27, v31, s[4:5]
	v_mul_f32_e32 v30, 0x37800000, v27
	v_cndmask_b32_e32 v27, v27, v30, vcc
	v_cmp_class_f32_e32 vcc, v26, v39
	s_nop 1
	v_cndmask_b32_e32 v26, v27, v26, vcc
	v_div_scale_f32 v27, s[4:5], v26, v26, 1.0
	v_rcp_f32_e32 v31, v27
	v_div_scale_f32 v30, vcc, 1.0, v26, 1.0
	v_fma_f32 v40, -v27, v31, 1.0
	v_fmac_f32_e32 v31, v40, v31
	v_mul_f32_e32 v40, v30, v31
	v_fma_f32 v41, -v27, v40, v30
	v_fmac_f32_e32 v40, v41, v31
	v_fma_f32 v27, -v27, v40, v30
	v_div_fmas_f32 v27, v27, v31, v40
	v_div_fixup_f32 v26, v27, v26, 1.0
	v_pk_mul_f32 v[24:25], v[24:25], v[26:27] op_sel_hi:[1,0]
	v_pk_mul_f32 v[26:27], v[28:29], v[26:27] op_sel_hi:[1,0]
	v_mov_b64_e32 v[2:3], v[100:101]
	v_mov_b64_e32 v[4:5], v[102:103]
	v_pk_mul_f32 v[4:5], v[4:5], v[24:25]
	v_pk_mul_f32 v[2:3], v[2:3], v[26:27]
	s_nop 0
	v_pk_mul_f32 v[2:3], v[2:3], s[44:45] op_sel_hi:[1,0]
	s_nop 0
	v_mul_f32_e32 v2, 0x41800000, v2
	v_mul_f32_e32 v3, 0x41800000, v3
	v_cvt_pk_fp8_f32 v42, v2, v3
	v_pk_mul_f32 v[2:3], v[4:5], s[44:45] op_sel_hi:[1,0]
	s_nop 0
	v_mul_f32_e32 v2, 0x41800000, v2
	v_mul_f32_e32 v3, 0x41800000, v3
	v_cvt_pk_fp8_f32 v42, v2, v3 op_sel:[0,0,1]
	global_store_dword v[22:23], v42, off offset:768
	s_cbranch_scc1 .LBB0_661
